# baseline (speedup 1.0000x reference)
.LBB0_3:
	s_setprio 2
	s_load_dwordx8 s[8:15], s[0:1], 0x0
	v_and_b32_e32 v199, 15, v0
	v_lshrrev_b32_e32 v206, 4, v1
	s_cmpk_gt_u32 s38, 0x17f
	v_lshlrev_b32_e32 v205, 2, v206
	v_lshlrev_b32_e32 v194, 4, v206
	s_mul_i32 s37, s3, 0xc8
	v_lshl_or_b32 v204, s36, 4, v199
	s_cbranch_scc0 .LBB0_52
	s_add_i32 s39, s36, -6
	s_lshl_b32 s4, s33, 7
	s_waitcnt lgkmcnt(0)
	s_add_u32 s40, s20, s4
	s_addc_u32 s41, s21, 0
	s_add_u32 s6, s24, s4
	s_addc_u32 s7, s25, 0
	s_lshl_b32 s24, s39, 4
	v_or_b32_e32 v131, s24, v199
	v_min_u32_e32 v2, 0xc7, v131
	v_add_u32_e32 v2, s37, v2
	v_ashrrev_i32_e32 v3, 31, v2
	v_lshlrev_b64 v[2:3], 2, v[2:3]
	s_add_i32 s21, s36, -4
	v_lshl_add_u64 v[4:5], s[8:9], 0, v[2:3]
	v_lshl_add_u64 v[2:3], s[10:11], 0, v[2:3]
	v_lshl_or_b32 v201, s21, 4, v199
	global_load_dword v35, v[2:3], off
	v_min_u32_e32 v2, 0xc7, v201
	v_add_u32_e32 v2, s37, v2
	v_ashrrev_i32_e32 v3, 31, v2
	v_lshlrev_b64 v[2:3], 2, v[2:3]
	global_load_dword v34, v[4:5], off
	v_lshl_add_u64 v[4:5], s[8:9], 0, v[2:3]
	v_lshl_add_u64 v[2:3], s[10:11], 0, v[2:3]
	global_load_dword v36, v[4:5], off
	global_load_dword v37, v[2:3], off
	v_mov_b32_e32 v195, 0
	v_lshlrev_b32_e32 v42, 4, v0
	v_mov_b32_e32 v43, v195
	s_movk_i32 s20, 0x2000
	v_lshl_add_u64 v[10:11], s[34:35], 0, v[42:43]
	v_add_co_u32_e32 v20, vcc, s20, v10
	s_movk_i32 s42, 0x4000
	s_nop 0
	v_addc_co_u32_e32 v21, vcc, 0, v11, vcc
	v_lshlrev_b32_e32 v6, 6, v0
	v_add_co_u32_e32 v22, vcc, s42, v10
	s_movk_i32 s43, 0x6000
	v_and_b32_e32 v6, 0x7e00, v6
	v_mov_b32_e32 v7, v195
	v_addc_co_u32_e32 v23, vcc, 0, v11, vcc
	s_mov_b32 s5, 0
	global_load_dwordx4 v[2:5], v42, s[34:35]
	v_mov_b32_e32 v9, v195
	v_lshl_add_u64 v[12:13], s[18:19], 0, v[6:7]
	v_or_b32_e32 v8, 0x8000, v6
	v_lshl_add_u64 v[6:7], s[22:23], 0, v[6:7]
	v_add_co_u32_e32 v24, vcc, s43, v10
	global_load_dwordx4 v[118:121], v194, s[40:41]
	global_load_dwordx4 v[114:117], v194, s[40:41] offset:64
	v_addc_co_u32_e32 v25, vcc, 0, v11, vcc
	v_lshl_add_u64 v[26:27], v[12:13], 0, s[4:5]
	v_lshl_add_u64 v[28:29], s[18:19], 0, v[8:9]
	v_lshl_add_u64 v[30:31], v[6:7], 0, s[4:5]
	v_lshl_add_u64 v[32:33], s[22:23], 0, v[8:9]
	global_load_dwordx4 v[6:9], v[20:21], off
	global_load_dwordx4 v[10:13], v[22:23], off
	global_load_dwordx4 v[14:17], v[24:25], off
	v_and_b32_e32 v18, 0x70, v42
	v_mov_b32_e32 v19, v195
	v_lshl_add_u64 v[38:39], v[26:27], 0, v[18:19]
	v_lshl_add_u64 v[20:21], v[28:29], 0, s[4:5]
	v_lshl_add_u64 v[22:23], v[32:33], 0, s[4:5]
	v_lshl_add_u64 v[40:41], v[30:31], 0, v[18:19]
	global_load_dwordx4 v[126:129], v194, s[6:7]
	global_load_dwordx4 v[122:125], v194, s[6:7] offset:64
	v_lshl_add_u64 v[44:45], v[20:21], 0, v[18:19]
	v_lshl_add_u64 v[46:47], v[22:23], 0, v[18:19]
	global_load_dwordx4 v[18:21], v[38:39], off
	global_load_dwordx4 v[22:25], v[44:45], off
	global_load_dwordx4 v[26:29], v[40:41], off
	global_load_dwordx4 v[30:33], v[46:47], off
	s_movk_i32 s25, 0x2710
	s_add_i32 s20, s36, -2
	v_lshl_or_b32 v207, s20, 4, v199
	v_min_u32_e32 v43, 0xc7, v207
	v_and_b32_e32 v42, 48, v42
	v_lshlrev_b32_e32 v48, 2, v0
	s_waitcnt vmcnt(14)
	v_mad_u64_u32 v[34:35], s[4:5], v35, s25, v[34:35]
	v_ashrrev_i32_e32 v35, 31, v34
	v_lshlrev_b64 v[34:35], 9, v[34:35]
	s_waitcnt vmcnt(12)
	v_mad_u64_u32 v[36:37], s[4:5], v37, s25, v[36:37]
	v_ashrrev_i32_e32 v37, 31, v36
	v_lshlrev_b64 v[44:45], 9, v[36:37]
	v_lshl_add_u64 v[34:35], s[14:15], 0, v[34:35]
	v_lshl_add_u64 v[44:45], s[14:15], 0, v[44:45]
	v_lshl_add_u64 v[46:47], v[34:35], 0, v[194:195]
	v_lshl_add_u64 v[44:45], v[44:45], 0, v[194:195]
	global_load_dwordx4 v[34:37], v[46:47], off
	global_load_dwordx4 v[38:41], v[46:47], off offset:64
	global_load_dwordx4 v[54:57], v[46:47], off offset:128
	global_load_dwordx4 v[82:85], v[46:47], off offset:192
	global_load_dwordx4 v[86:89], v[46:47], off offset:256
	global_load_dwordx4 v[90:93], v[46:47], off offset:320
	global_load_dwordx4 v[94:97], v[46:47], off offset:384
	global_load_dwordx4 v[98:101], v[46:47], off offset:448
	global_load_dwordx4 v[158:161], v[44:45], off
	global_load_dwordx4 v[154:157], v[44:45], off offset:64
	global_load_dwordx4 v[150:153], v[44:45], off offset:128
	global_load_dwordx4 v[146:149], v[44:45], off offset:192
	global_load_dwordx4 v[66:69], v[44:45], off offset:256
	global_load_dwordx4 v[70:73], v[44:45], off offset:320
	global_load_dwordx4 v[74:77], v[44:45], off offset:384
	global_load_dwordx4 v[78:81], v[44:45], off offset:448
	v_add_u32_e32 v44, s37, v43
	v_ashrrev_i32_e32 v45, 31, v44
	v_lshlrev_b64 v[44:45], 2, v[44:45]
	v_lshl_add_u64 v[46:47], s[8:9], 0, v[44:45]
	v_lshl_add_u64 v[44:45], s[10:11], 0, v[44:45]
	global_load_dword v140, v[46:47], off
	global_load_dword v135, v[44:45], off
	v_min_u32_e32 v43, 0xc7, v204
	v_add_u32_e32 v44, s37, v43
	v_ashrrev_i32_e32 v45, 31, v44
	s_add_i32 s4, s24, 0x80
	v_lshlrev_b64 v[44:45], 2, v[44:45]
	v_or_b32_e32 v43, s4, v199
	v_lshl_add_u64 v[46:47], s[8:9], 0, v[44:45]
	v_lshl_add_u64 v[44:45], s[10:11], 0, v[44:45]
	v_min_u32_e32 v43, 0xc7, v43
	global_load_dword v133, v[44:45], off
	v_add_u32_e32 v44, s37, v43
	v_ashrrev_i32_e32 v45, 31, v44
	v_lshlrev_b64 v[44:45], 2, v[44:45]
	global_load_dword v130, v[46:47], off
	v_lshl_add_u64 v[46:47], s[8:9], 0, v[44:45]
	v_lshl_add_u64 v[44:45], s[10:11], 0, v[44:45]
	global_load_dword v134, v[44:45], off
	v_lshlrev_b32_e32 v45, 3, v0
	v_lshrrev_b32_e32 v43, 5, v0
	v_and_b32_e32 v44, 4, v0
	v_and_b32_e32 v45, 0xc0, v45
	v_or3_b32 v42, v42, v43, v45
	v_lshlrev_b32_e32 v43, 1, v44
	s_waitcnt vmcnt(32)
	v_cvt_pk_f16_f32 v2, v2, v3
	v_cvt_pk_f16_f32 v3, v4, v5
	v_lshl_or_b32 v42, v42, 4, v43
	s_waitcnt vmcnt(29)
	v_cvt_pk_f16_f32 v4, v6, v7
	v_cvt_pk_f16_f32 v5, v8, v9
	ds_write2st64_b64 v42, v[2:3], v[4:5] offset0:101 offset1:109
	s_waitcnt vmcnt(28)
	v_cvt_pk_f16_f32 v2, v10, v11
	v_cvt_pk_f16_f32 v3, v12, v13
	s_waitcnt vmcnt(27)
	v_cvt_pk_f16_f32 v4, v14, v15
	v_cvt_pk_f16_f32 v5, v16, v17
	ds_write2st64_b64 v42, v[2:3], v[4:5] offset0:117 offset1:125
	v_lshrrev_b32_e32 v4, 2, v0
	v_lshrrev_b32_e32 v2, 1, v0
	v_lshrrev_b32_e32 v3, 4, v0
	v_and_b32_e32 v4, 6, v4
	v_and_b32_e32 v2, 48, v2
	v_and_or_b32 v3, v3, 8, v4
	v_lshrrev_b32_e32 v4, 8, v0
	v_and_or_b32 v2, v48, 12, v2
	v_or_b32_e32 v4, v4, v44
	s_waitcnt vmcnt(24)
	v_cvt_f16_f32_e32 v5, v18
	v_lshlrev_b32_e32 v4, 10, v4
	v_lshlrev_b32_e32 v2, 4, v2
	v_or3_b32 v2, v2, v4, v3
	v_cvt_f16_f32_e32 v3, v19
	v_cvt_f16_f32_e32 v4, v20
	v_add_u32_e32 v2, 0x10a00, v2
	v_cvt_f16_f32_e32 v6, v21
	global_load_dword v132, v[46:47], off
	ds_write_b16 v2, v5
	ds_write_b16 v2, v3 offset:16
	ds_write_b16 v2, v4 offset:32
	ds_write_b16 v2, v6 offset:48
	s_waitcnt vmcnt(24)
	v_cvt_f16_f32_e32 v3, v22
	v_cvt_f16_f32_e32 v4, v23
	v_cvt_f16_f32_e32 v5, v24
	v_cvt_f16_f32_e32 v6, v25
	ds_write_b16 v2, v3 offset:2048
	ds_write_b16 v2, v4 offset:2064
	ds_write_b16 v2, v5 offset:2080
	ds_write_b16 v2, v6 offset:2096
	s_waitcnt vmcnt(23)
	v_cvt_f16_f32_e32 v3, v26
	v_cvt_f16_f32_e32 v4, v27
	v_cvt_f16_f32_e32 v5, v28
	v_cvt_f16_f32_e32 v6, v29
	ds_write_b16 v2, v3 offset:8192
	ds_write_b16 v2, v4 offset:8208
	ds_write_b16 v2, v5 offset:8224
	ds_write_b16 v2, v6 offset:8240
	s_waitcnt vmcnt(22)
	v_cvt_f16_f32_e32 v3, v30
	v_cvt_f16_f32_e32 v4, v31
	v_cvt_f16_f32_e32 v5, v32
	v_cvt_f16_f32_e32 v6, v33
	ds_write_b16 v2, v3 offset:10240
	ds_write_b16 v2, v4 offset:10256
	ds_write_b16 v2, v5 offset:10272
	ds_write_b16 v2, v6 offset:10288
	v_mov_b32_e32 v2, 0x10a00
	s_waitcnt lgkmcnt(0)
	s_barrier
	v_lshl_add_u32 v141, v1, 4, v2
	ds_read_b128 v[6:9], v141
	ds_read_b128 v[2:5], v141 offset:1024
	ds_read_b128 v[10:13], v141 offset:4096
	ds_read_b128 v[14:17], v141 offset:8192
	s_waitcnt vmcnt(21)
	v_cvt_pk_f16_f32 v102, v34, v35
	v_cvt_pk_f16_f32 v103, v36, v37
	s_waitcnt vmcnt(20)
	v_cvt_pk_f16_f32 v104, v38, v39
	v_cvt_pk_f16_f32 v105, v40, v41
	ds_read_b128 v[26:29], v141 offset:2048
	ds_read_b128 v[18:21], v141 offset:3072
	ds_read_b128 v[46:49], v141 offset:5120
	ds_read_b128 v[58:61], v141 offset:12288
	s_waitcnt lgkmcnt(7)
	v_mfma_f32_16x16x32_f16 v[38:41], v[6:9], v[102:105], 0
	s_waitcnt vmcnt(19)
	v_cvt_pk_f16_f32 v136, v54, v55
	v_cvt_pk_f16_f32 v137, v56, v57
	s_waitcnt vmcnt(18)
	v_cvt_pk_f16_f32 v138, v82, v83
	s_waitcnt lgkmcnt(5)
	v_mfma_f32_16x16x32_f16 v[106:109], v[10:13], v[102:105], 0
	v_cvt_pk_f16_f32 v139, v84, v85
	ds_read_b128 v[34:37], v141 offset:6144
	ds_read_b128 v[22:25], v141 offset:7168
	ds_read_b128 v[50:53], v141 offset:9216
	ds_read_b128 v[42:45], v141 offset:10240
	ds_read_b128 v[30:33], v141 offset:11264
	ds_read_b128 v[62:65], v141 offset:13312
	v_mfma_f32_16x16x32_f16 v[82:85], v[2:5], v[136:139], v[38:41]
	ds_read_b128 v[54:57], v141 offset:14336
	s_nop 1
	ds_read_b128 v[38:41], v141 offset:15360
	s_waitcnt vmcnt(4)
	v_mad_u64_u32 v[144:145], s[4:5], v135, s25, v[140:141]
	s_waitcnt lgkmcnt(12)
	v_mfma_f32_16x16x32_f16 v[110:113], v[14:17], v[102:105], 0
	v_cvt_pk_f16_f32 v140, v86, v87
	v_cvt_pk_f16_f32 v141, v88, v89
	v_cvt_pk_f16_f32 v142, v90, v91
	s_waitcnt lgkmcnt(8)
	v_mfma_f32_16x16x32_f16 v[102:105], v[58:61], v[102:105], 0
	v_cvt_pk_f16_f32 v143, v92, v93
	v_cvt_pk_f16_f32 v164, v98, v99
	v_cvt_pk_f16_f32 v165, v100, v101
	v_mfma_f32_16x16x32_f16 v[106:109], v[46:49], v[136:139], v[106:109]
	s_add_i32 s4, s24, 0xa0
	v_ashrrev_i32_e32 v145, 31, v144
	v_cvt_pk_f16_f32 v162, v94, v95
	v_mfma_f32_16x16x32_f16 v[98:101], v[26:29], v[140:143], v[82:85]
	v_cvt_pk_f16_f32 v163, v96, v97
	s_waitcnt lgkmcnt(5)
	v_mfma_f32_16x16x32_f16 v[86:89], v[50:53], v[136:139], v[110:113]
	v_lshlrev_b64 v[82:83], 9, v[144:145]
	v_lshl_add_u64 v[82:83], s[14:15], 0, v[82:83]
	v_lshl_add_u64 v[94:95], v[82:83], 0, v[194:195]
	s_waitcnt lgkmcnt(2)
	v_mfma_f32_16x16x32_f16 v[102:105], v[62:65], v[136:139], v[102:105]
	global_load_dwordx4 v[190:193], v[94:95], off
	global_load_dwordx4 v[186:189], v[94:95], off offset:64
	global_load_dwordx4 v[182:185], v[94:95], off offset:128
	global_load_dwordx4 v[178:181], v[94:95], off offset:192
	v_mfma_f32_16x16x32_f16 v[110:113], v[34:37], v[140:143], v[106:109]
	s_nop 2
	v_or_b32_e32 v106, s4, v199
	v_min_u32_e32 v135, 0xc7, v106
	v_mfma_f32_16x16x32_f16 v[106:109], v[18:21], v[162:165], v[98:101]
	s_movk_i32 s4, 0xc8
	v_cmp_gt_u32_e32 vcc, s4, v131
	s_nop 0
	v_add_u32_e32 v98, s37, v135
	v_ashrrev_i32_e32 v99, 31, v98
	v_mfma_f32_16x16x32_f16 v[136:139], v[42:45], v[140:143], v[86:89]
	global_load_dwordx4 v[82:85], v[94:95], off offset:256
	s_nop 1
	global_load_dwordx4 v[86:89], v[94:95], off offset:320
	global_load_dwordx4 v[90:93], v[94:95], off offset:384
	s_nop 0
	global_load_dwordx4 v[94:97], v[94:95], off offset:448
	s_waitcnt lgkmcnt(1)
	v_mfma_f32_16x16x32_f16 v[102:105], v[54:57], v[140:143], v[102:105]
	v_lshlrev_b64 v[140:141], 2, v[98:99]
	v_mfma_f32_16x16x32_f16 v[98:101], v[22:25], v[162:165], v[110:113]
	s_nop 2
	v_lshl_add_u64 v[110:111], s[8:9], 0, v[140:141]
	v_lshl_add_u64 v[140:141], s[10:11], 0, v[140:141]
	global_load_dword v200, v[110:111], off
	global_load_dword v208, v[140:141], off
	v_mfma_f32_16x16x32_f16 v[110:113], v[30:33], v[162:165], v[136:139]
	s_waitcnt lgkmcnt(0)
	v_mfma_f32_16x16x32_f16 v[102:105], v[38:41], v[162:165], v[102:105]
	s_and_saveexec_b64 s[4:5], vcc
	s_cbranch_execz .LBB0_6
	v_mul_f32_e32 v135, 0xbfb8aa3b, v118
	v_fmac_f32_e32 v135, 0xbfb8aa3b, v106
	v_exp_f32_e32 v106, v135
	v_mul_f32_e32 v135, 0x4038aa3b, v126
	v_fmac_f32_e32 v135, 0x4038aa3b, v110
	v_exp_f32_e32 v110, v135
	v_add_f32_e32 v106, 1.0, v106
	v_rcp_f32_e32 v135, v106
	s_movk_i32 s6, 0xca0
	v_add_f32_e32 v106, 1.0, v110
	v_mul_f32_e32 v110, 0xbfb8aa3b, v114
	v_fmac_f32_e32 v110, 0xbfb8aa3b, v98
	v_exp_f32_e32 v98, v110
	v_mul_f32_e32 v110, 0x4038aa3b, v122
	v_fmac_f32_e32 v110, 0x4038aa3b, v102
	v_exp_f32_e32 v102, v110
	v_add_f32_e32 v98, 1.0, v98
	v_rcp_f32_e32 v110, v98
	v_rcp_f32_e32 v106, v106
	v_add_f32_e32 v98, 1.0, v102
	v_mul_f32_e32 v102, 0xbfb8aa3b, v119
	v_fmac_f32_e32 v102, 0xbfb8aa3b, v107
	v_mul_f32_e32 v107, 0x4038aa3b, v127
	v_exp_f32_e32 v102, v102
	v_fmac_f32_e32 v107, 0x4038aa3b, v111
	v_exp_f32_e32 v107, v107
	v_rcp_f32_e32 v98, v98
	v_add_f32_e32 v102, 1.0, v102
	v_rcp_f32_e32 v111, v102
	v_add_f32_e32 v102, 1.0, v107
	v_rcp_f32_e32 v107, v102
	v_mul_f32_e32 v102, 0xbfb8aa3b, v115
	v_fmac_f32_e32 v102, 0xbfb8aa3b, v99
	v_exp_f32_e32 v99, v102
	v_mul_f32_e32 v102, 0x4038aa3b, v123
	v_fmac_f32_e32 v102, 0x4038aa3b, v103
	v_exp_f32_e32 v136, v102
	v_pk_fma_f32 v[102:103], v[106:107], -2.0, 1.0 op_sel_hi:[1,0,0]
	v_mul_f32_e32 v106, 0xbfb8aa3b, v120
	v_fmac_f32_e32 v106, 0xbfb8aa3b, v108
	v_mul_f32_e32 v107, 0x4038aa3b, v128
	v_exp_f32_e32 v106, v106
	v_fmac_f32_e32 v107, 0x4038aa3b, v112
	v_exp_f32_e32 v107, v107
	v_add_f32_e32 v99, 1.0, v99
	v_add_f32_e32 v106, 1.0, v106
	v_rcp_f32_e32 v108, v106
	v_add_f32_e32 v106, 1.0, v107
	v_mul_f32_e32 v107, 0xbfb8aa3b, v116
	v_fmac_f32_e32 v107, 0xbfb8aa3b, v100
	v_exp_f32_e32 v100, v107
	v_mul_f32_e32 v107, 0x4038aa3b, v124
	v_fmac_f32_e32 v107, 0x4038aa3b, v104
	v_exp_f32_e32 v104, v107
	v_add_f32_e32 v100, 1.0, v100
	v_rcp_f32_e32 v112, v100
	v_mul_f32_e32 v107, 0x4038aa3b, v129
	v_add_f32_e32 v100, 1.0, v104
	v_mul_f32_e32 v104, 0xbfb8aa3b, v121
	v_fmac_f32_e32 v104, 0xbfb8aa3b, v109
	v_exp_f32_e32 v104, v104
	v_fmac_f32_e32 v107, 0x4038aa3b, v113
	v_exp_f32_e32 v107, v107
	v_rcp_f32_e32 v106, v106
	v_add_f32_e32 v104, 1.0, v104
	v_rcp_f32_e32 v109, v104
	v_add_f32_e32 v104, 1.0, v107
	v_rcp_f32_e32 v107, v104
	v_mul_f32_e32 v104, 0x4038aa3b, v125
	v_fmac_f32_e32 v104, 0x4038aa3b, v105
	v_mul_f32_e32 v105, 0xbfb8aa3b, v117
	v_exp_f32_e32 v104, v104
	v_fmac_f32_e32 v105, 0xbfb8aa3b, v101
	v_exp_f32_e32 v113, v105
	v_rcp_f32_e32 v137, v99
	v_add_f32_e32 v99, 1.0, v136
	v_add_f32_e32 v101, 1.0, v104
	v_rcp_f32_e32 v99, v99
	v_rcp_f32_e32 v100, v100
	v_rcp_f32_e32 v101, v101
	v_pk_fma_f32 v[104:105], v[106:107], -2.0, 1.0 op_sel_hi:[1,0,0]
	v_add_f32_e32 v106, 1.0, v113
	v_rcp_f32_e32 v113, v106
	v_cvt_pk_f16_f32 v107, v102, v103
	v_lshlrev_b32_e32 v102, 3, v131
	v_cvt_pk_f16_f32 v106, v135, v111
	v_mad_u32_u24 v111, v206, s6, v102
	v_pk_fma_f32 v[98:99], v[98:99], -2.0, 1.0 op_sel_hi:[1,0,0]
	v_pk_fma_f32 v[100:101], v[100:101], -2.0, 1.0 op_sel_hi:[1,0,0]
	v_cvt_pk_f16_f32 v102, v108, v109
	v_cvt_pk_f16_f32 v103, v104, v105
	v_add_u32_e32 v104, 0x6400, v111
	ds_write2_b64 v104, v[106:107], v[102:103] offset0:32 offset1:234
	v_cvt_pk_f16_f32 v102, v110, v137
	v_cvt_pk_f16_f32 v103, v98, v99
	v_cvt_pk_f16_f32 v98, v112, v113
	v_cvt_pk_f16_f32 v99, v100, v101
	v_add_u32_e32 v100, 0x9600, v111
	ds_write2_b64 v100, v[102:103], v[98:99] offset0:48 offset1:250

.LBB0_86:
	s_or_b64 exec, exec, s[0:1]
	v_cmp_ne_u32_e32 vcc, 0, v14
	s_waitcnt lgkmcnt(0)
	s_barrier
	s_setprio 0
	v_and_b32_e32 v40, 15, v1
	v_lshrrev_b32_e32 v41, 4, v1
	s_and_b32 s44, s36, 1
	s_lshr_b32 s45, s36, 1
	s_mov_b32 s60, 0xffff
	s_mov_b32 s61, 0
	s_mov_b32 s62, 0xffff0000
	s_mov_b32 s63, 0
	s_mov_b32 s64, 0
	s_mov_b32 s65, 0xffff
	s_mov_b32 s66, 0
	s_mov_b32 s67, 0xffff0000
	v_cvt_pk_f16_f32 v2, v152, v153
	v_cvt_pk_f16_f32 v3, v154, v155
	v_cvt_pk_f16_f32 v4, v156, v157
	v_cvt_pk_f16_f32 v5, v158, v159
	s_lshl_b32 s46, s44, 3
	v_lshl_add_u32 v42, v41, 1, s46
	v_mul_u32_u24_e32 v32, 0x650, v42
	v_lshl_add_u32 v34, v40, 3, v32
	v_mul_u32_u24_e32 v33, 0x650, v40
	v_add_u32_e32 v33, 0x6500, v33
	s_lshl_b32 s47, s45, 1
	v_lshl_add_u32 v35, v40, 2, s47
	v_lshl_add_u32 v35, v41, 8, v35
	s_lshl_b32 s46, s3, 2
	s_add_i32 s46, s46, s33
	s_lshl_b32 s46, s46, 1
	s_add_i32 s46, s46, s44
	s_mul_i32 s46, s46, 0x3200
	s_add_u32 s68, s26, s46
	s_addc_u32 s69, s27, 0
	v_mov_b32_e32 v36, 0x14a00
